# P10 expert down GEMM walks the row blocks in reverse (highest first): the activation rows P9 wrote last are read first
# speedup vs baseline: 1.4327x; 1.0008x over previous
.LBB0_1429:
	s_add_i32 s0, 0, 0x210c0
	s_waitcnt vmcnt(2)
	v_mov_b32_e32 v10, v0
	v_mov_b32_e32 v1, s0
	ds_read_b32 v1, v1
	s_and_b32 s0, s54, 24
	s_add_i32 s0, s0, s55
	v_readfirstlane_b32 s22, v10
	s_waitcnt lgkmcnt(0)
	v_cmp_ge_i32_e32 vcc, s0, v1
	s_cbranch_vccnz .LBB0_1449
	s_mov_b32 s98, s0
	v_readfirstlane_b32 s99, v1
	s_sub_i32 s0, s99, s0
	s_add_i32 s0, s0, -1
	v_lshlrev_b32_e32 v1, 4, v10
	s_waitcnt vmcnt(1)
	v_add_u32_e32 v2, 0x2000, v1
	v_ashrrev_i32_e32 v3, 31, v2
	v_lshrrev_b32_e32 v3, 22, v3
	v_add_u32_e32 v3, v2, v3
	v_ashrrev_i32_e32 v3, 10, v3
	v_mul_i32_i24_e32 v4, 0x400, v3
	v_sub_u32_e32 v2, v2, v4
	v_lshrrev_b32_e32 v4, 4, v2
	v_bitop3_b32 v2, v4, v2, 32 bitop3:0x6c
	v_ashrrev_i32_e32 v4, 31, v2
	v_lshrrev_b32_e32 v4, 26, v4
	v_add_u32_e32 v4, v2, v4
	v_ashrrev_i32_e32 v5, 6, v4
	v_and_b32_e32 v4, 0xc0, v4
	v_sub_u32_e32 v2, v2, v4
	v_mov_b32_e32 v4, 1
	s_waitcnt vmcnt(0)
	v_lshlrev_b32_e32 v6, 3, v3
	v_lshlrev_b32_e32 v3, 5, v3
	v_ashrrev_i16_sdwa v2, v4, sext(v2) dst_sel:DWORD dst_unused:UNUSED_PAD src0_sel:DWORD src1_sel:BYTE_0
	v_and_b32_e32 v3, 32, v3
	v_bfe_i32 v2, v2, 0, 16
	v_add_lshl_u32 v12, v3, v2, 1
	v_bfe_i32 v2, v10, 27, 1
	s_add_u32 s31, s6, 0x32000000
	v_lshrrev_b32_e32 v2, 22, v2
	s_addc_u32 s52, s7, 0
	v_add_u32_e32 v2, v1, v2
	s_add_u32 s53, s6, 0x76000000
	v_and_b32_e32 v6, -16, v6
	v_and_b32_e32 v2, 0xfffffc00, v2
	s_addc_u32 s55, s7, 0
	s_and_b32 s1, s54, 4
	v_add_u32_e32 v11, v5, v6
	v_sub_u32_e32 v1, v1, v2
	v_ashrrev_i32_e32 v3, 31, v10
	s_or_b32 s10, s1, s33
	v_and_b32_e32 v5, 3, v5
	s_mov_b32 s1, 0x1fffe0
	v_lshrrev_b32_e32 v6, 2, v11
	v_lshlrev_b32_e32 v7, 1, v11
	v_lshrrev_b32_e32 v2, 4, v1
	v_lshrrev_b32_e32 v3, 26, v3
	v_and_or_b32 v5, v11, s1, v5
	v_and_b32_e32 v6, 4, v6
	v_and_b32_e32 v7, 24, v7
	v_bitop3_b32 v2, v2, v1, 32 bitop3:0x6c
	v_ashrrev_i32_e32 v1, 31, v1
	v_add_u32_e32 v3, v10, v3
	v_or3_b32 v5, v5, v6, v7
	v_lshrrev_b32_e32 v1, 26, v1
	v_ashrrev_i32_e32 v3, 6, v3
	v_lshl_add_u32 v162, v5, 11, v12
	v_add_u32_e32 v1, v2, v1
	v_lshlrev_b32_e32 v5, 3, v3
	v_ashrrev_i32_e32 v1, 6, v1
	v_and_b32_e32 v5, -16, v5
	v_add_u32_e32 v13, v1, v5
	v_and_b32_e32 v5, 3, v1
	v_mul_i32_i24_e32 v1, 64, v1
	v_sub_u32_e32 v1, v2, v1
	v_and_or_b32 v5, v13, s1, v5
	v_lshlrev_b32_e32 v3, 5, v3
	v_ashrrev_i16_sdwa v1, v4, sext(v1) dst_sel:DWORD dst_unused:UNUSED_PAD src0_sel:DWORD src1_sel:BYTE_0
	s_add_i32 s1, 0, 0x21044
	v_and_b32_e32 v3, 32, v3
	v_bfe_i32 v1, v1, 0, 16
	v_mov_b32_e32 v2, s1
	v_lshrrev_b32_e32 v6, 2, v13
	v_lshlrev_b32_e32 v7, 1, v13
	v_add_lshl_u32 v1, v3, v1, 1
	ds_read2_b32 v[2:3], v2 offset1:1
	s_add_i32 s1, 0, 0x2104c
	v_and_b32_e32 v6, 4, v6
	v_and_b32_e32 v7, 24, v7
	v_mov_b32_e32 v4, s1
	s_add_i32 s1, 0, 0x21054
	v_or3_b32 v5, v5, v6, v7
	v_mov_b32_e32 v6, s1
	s_add_i32 s1, 0, 0x2105c
	v_mov_b32_e32 v8, s1
	v_lshl_add_u32 v164, v5, 11, v1
	ds_read2_b32 v[4:5], v4 offset1:1
	ds_read2_b32 v[6:7], v6 offset1:1
	ds_read2_b32 v[8:9], v8 offset1:1
	s_waitcnt lgkmcnt(3)
	v_cmp_ge_i32_e32 vcc, s0, v2
	s_add_i32 s1, 0, 0x21064
	s_ashr_i32 s20, s22, 6
	v_cndmask_b32_e64 v2, 0, 1, vcc
	v_cmp_ge_i32_e32 vcc, s0, v3
	s_ashr_i32 s11, s10, 31
	s_ashr_i32 s23, s22, 8
	v_cndmask_b32_e64 v3, 0, 1, vcc
	s_waitcnt lgkmcnt(2)
	v_cmp_ge_i32_e32 vcc, s0, v4
	s_lshl_b32 s56, s20, 10
	s_lshl_b64 s[16:17], s[10:11], 19
	v_addc_co_u32_e32 v2, vcc, v3, v2, vcc
	v_cmp_ge_i32_e32 vcc, s0, v5
	v_lshl_add_u32 v166, v13, 11, v1
	v_lshl_add_u32 v168, v11, 11, v12
	v_cndmask_b32_e64 v3, 0, 1, vcc
	s_waitcnt lgkmcnt(1)
	v_cmp_ge_i32_e32 vcc, s0, v6
	v_add_u32_e32 v170, 0x40000, v166
	v_add_u32_e32 v172, 0x40000, v168
	v_addc_co_u32_e32 v2, vcc, v2, v3, vcc
	v_cmp_ge_i32_e32 vcc, s0, v7
	v_mov_b32_e32 v165, 0
	v_mov_b32_e32 v163, v165
	v_cndmask_b32_e64 v3, 0, 1, vcc
	s_waitcnt lgkmcnt(0)
	v_cmp_ge_i32_e32 vcc, s0, v8
	v_mov_b32_e32 v167, v165
	v_mov_b32_e32 v169, v165
	v_addc_co_u32_e32 v14, vcc, v2, v3, vcc
	v_mov_b32_e32 v2, s1
	ds_read2_b32 v[2:3], v2 offset1:1
	s_add_i32 s1, 0, 0x2106c
	v_mov_b32_e32 v4, s1
	s_add_i32 s1, 0, 0x21074
	v_mov_b32_e32 v6, s1
	s_add_i32 s1, 0, 0x2107c
	v_cmp_ge_i32_e32 vcc, s0, v9
	v_mov_b32_e32 v8, s1
	ds_read2_b32 v[4:5], v4 offset1:1
	ds_read2_b32 v[6:7], v6 offset1:1
	ds_read2_b32 v[8:9], v8 offset1:1
	v_cndmask_b32_e64 v15, 0, 1, vcc
	s_waitcnt lgkmcnt(3)
	v_cmp_ge_i32_e32 vcc, s0, v2
	s_add_i32 s1, 0, 0x21084
	s_mov_b32 s58, 0x40000
	v_addc_co_u32_e32 v2, vcc, v14, v15, vcc
	v_cmp_ge_i32_e32 vcc, s0, v3
	s_nop 1
	v_cndmask_b32_e64 v3, 0, 1, vcc
	s_waitcnt lgkmcnt(2)
	v_cmp_ge_i32_e32 vcc, s0, v4
	s_nop 1
	v_addc_co_u32_e32 v2, vcc, v2, v3, vcc
	v_cmp_ge_i32_e32 vcc, s0, v5
	s_nop 1
	v_cndmask_b32_e64 v3, 0, 1, vcc
	s_waitcnt lgkmcnt(1)
	v_cmp_ge_i32_e32 vcc, s0, v6
	s_nop 1
	v_addc_co_u32_e32 v2, vcc, v2, v3, vcc
	v_cmp_ge_i32_e32 vcc, s0, v7
	s_nop 1
	v_cndmask_b32_e64 v3, 0, 1, vcc
	s_waitcnt lgkmcnt(0)
	v_cmp_ge_i32_e32 vcc, s0, v8
	s_nop 1
	v_addc_co_u32_e32 v14, vcc, v2, v3, vcc
	v_mov_b32_e32 v2, s1
	ds_read2_b32 v[2:3], v2 offset1:1
	s_add_i32 s1, 0, 0x2108c
	v_mov_b32_e32 v4, s1
	s_add_i32 s1, 0, 0x21094
	v_mov_b32_e32 v6, s1
	s_add_i32 s1, 0, 0x2109c
	v_cmp_ge_i32_e32 vcc, s0, v9
	v_mov_b32_e32 v8, s1
	ds_read2_b32 v[4:5], v4 offset1:1
	ds_read2_b32 v[6:7], v6 offset1:1
	ds_read2_b32 v[8:9], v8 offset1:1
	v_cndmask_b32_e64 v15, 0, 1, vcc
	s_waitcnt lgkmcnt(3)
	v_cmp_ge_i32_e32 vcc, s0, v2
	s_add_i32 s1, 0, 0x210a4
	s_nop 0
	v_addc_co_u32_e32 v2, vcc, v14, v15, vcc
	v_cmp_ge_i32_e32 vcc, s0, v3
	s_nop 1
	v_cndmask_b32_e64 v3, 0, 1, vcc
	s_waitcnt lgkmcnt(2)
	v_cmp_ge_i32_e32 vcc, s0, v4
	s_nop 1
	v_addc_co_u32_e32 v2, vcc, v2, v3, vcc
	v_cmp_ge_i32_e32 vcc, s0, v5
	s_nop 1
	v_cndmask_b32_e64 v3, 0, 1, vcc
	s_waitcnt lgkmcnt(1)
	v_cmp_ge_i32_e32 vcc, s0, v6
	s_nop 1
	v_addc_co_u32_e32 v2, vcc, v2, v3, vcc
	v_cmp_ge_i32_e32 vcc, s0, v7
	s_nop 1
	v_cndmask_b32_e64 v3, 0, 1, vcc
	s_waitcnt lgkmcnt(0)
	v_cmp_ge_i32_e32 vcc, s0, v8
	s_nop 1
	v_addc_co_u32_e32 v8, vcc, v2, v3, vcc
	v_mov_b32_e32 v2, s1
	ds_read2_b32 v[2:3], v2 offset1:1
	s_add_i32 s1, 0, 0x210ac
	v_mov_b32_e32 v4, s1
	s_add_i32 s1, 0, 0x210b4
	v_mov_b32_e32 v6, s1
	s_add_i32 s1, 0, 0x210bc
	v_cmp_ge_i32_e32 vcc, s0, v9
	v_mov_b32_e32 v14, s1
	ds_read2_b32 v[4:5], v4 offset1:1
	ds_read2_b32 v[6:7], v6 offset1:1
	ds_read_b32 v14, v14
	v_cndmask_b32_e64 v9, 0, 1, vcc
	s_waitcnt lgkmcnt(3)
	v_cmp_ge_i32_e32 vcc, s0, v2
	s_ashr_i32 s1, s0, 31
	s_lshl_b64 s[12:13], s[0:1], 19
	v_addc_co_u32_e32 v2, vcc, v8, v9, vcc
	v_cmp_ge_i32_e32 vcc, s0, v3
	s_nop 1
	v_cndmask_b32_e64 v3, 0, 1, vcc
	s_waitcnt lgkmcnt(2)
	v_cmp_ge_i32_e32 vcc, s0, v4
	s_nop 1
	v_addc_co_u32_e32 v2, vcc, v2, v3, vcc
	v_cmp_ge_i32_e32 vcc, s0, v5
	s_nop 1
	v_cndmask_b32_e64 v3, 0, 1, vcc
	s_waitcnt lgkmcnt(1)
	v_cmp_ge_i32_e32 vcc, s0, v6
	s_nop 1
	v_addc_co_u32_e32 v2, vcc, v2, v3, vcc
	v_cmp_ge_i32_e32 vcc, s0, v7
	s_nop 1
	v_cndmask_b32_e64 v3, 0, 1, vcc
	s_waitcnt lgkmcnt(0)
	v_cmp_ge_i32_e32 vcc, s0, v14
	s_nop 1
	v_addc_co_u32_e32 v2, vcc, v2, v3, vcc
	s_nop 0
	v_readfirstlane_b32 s40, v2
	s_ashr_i32 s41, s40, 31
	s_lshl_b64 s[14:15], s[40:41], 22
	s_add_u32 s42, s31, s12
	s_addc_u32 s43, s52, s13
	s_add_u32 s1, s53, s14
	s_addc_u32 s11, s55, s15
	s_add_u32 s44, s1, s16
	s_addc_u32 s45, s11, s17
	s_add_i32 s1, s56, 0
	s_add_i32 m0, s1, 0x10000
	v_lshl_add_u64 v[8:9], s[44:45], 0, v[164:165]
	global_load_lds_dwordx4 v164, s[44:45]
	s_add_i32 m0, s1, 0x12000
	s_add_u32 s12, s44, 0x40000
	global_load_lds_dwordx4 v162, s[44:45]
	s_addc_u32 s13, s45, 0
	s_add_i32 m0, s1, 0x14000
	s_add_i32 s33, s1, 0x2000
	global_load_lds_dwordx4 v164, s[12:13]
	s_add_i32 m0, s1, 0x16000
	s_add_i32 s54, s1, 0x4000
	global_load_lds_dwordx4 v162, s[12:13]
	s_mov_b32 m0, s1
	s_add_i32 s57, s1, 0x6000
	global_load_lds_dwordx4 v166, s[42:43]
	s_mov_b32 m0, s33
	s_load_dwordx2 s[12:13], s[8:9], 0xe8
	global_load_lds_dwordx4 v168, s[42:43]
	s_mov_b32 m0, s54
	s_cmp_eq_u32 s23, 1
	global_load_lds_dwordx4 v170, s[42:43]
	s_mov_b32 m0, s57
	v_lshl_add_u64 v[4:5], s[44:45], 0, v[162:163]
	global_load_lds_dwordx4 v172, s[42:43]
	s_mov_b64 s[14:15], 0x40000
	v_lshl_add_u64 v[2:3], s[42:43], 0, v[166:167]
	s_cselect_b64 s[16:17], -1, 0
	s_cmp_lg_u32 s23, 1
	v_lshl_add_u64 v[6:7], s[42:43], 0, v[168:169]
	s_cbranch_scc1 .LBB0_1432
	s_barrier

.LBB0_1435:
	ds_read_b32 v2, v184
	s_add_i32 s62, s62, 1
	s_mul_i32 s6, s62, s59
	s_add_i32 s11, s98, s6
	s_waitcnt lgkmcnt(0)
	v_cmp_ge_i32_e64 s[8:9], s11, v2
	v_cmp_lt_i32_e64 s[6:7], s11, v2
	s_and_b64 vcc, exec, s[8:9]
	s_cbranch_vccnz .LBB0_1446
	s_sub_i32 s11, s99, s11
	s_add_i32 s11, s11, -1
	v_mov_b32_e32 v2, s63
	ds_read2_b32 v[2:3], v2 offset1:1
	v_mov_b32_e32 v4, s64
	v_mov_b32_e32 v6, s65
	v_mov_b32_e32 v8, s66
	ds_read2_b32 v[4:5], v4 offset1:1
	ds_read2_b32 v[6:7], v6 offset1:1
	ds_read2_b32 v[8:9], v8 offset1:1
	s_waitcnt lgkmcnt(0)
	v_cmp_ge_i32_e32 vcc, s11, v2
	s_mov_b32 s36, s11
	s_nop 0
	v_cndmask_b32_e64 v2, 0, 1, vcc
	v_cmp_ge_i32_e32 vcc, s11, v3
	s_nop 1
	v_cndmask_b32_e64 v3, 0, 1, vcc
	v_cmp_ge_i32_e32 vcc, s11, v4
	v_mov_b32_e32 v4, s68
	s_nop 0
	v_addc_co_u32_e32 v2, vcc, v3, v2, vcc
	v_cmp_ge_i32_e32 vcc, s11, v5
	s_nop 1
	v_cndmask_b32_e64 v3, 0, 1, vcc
	v_cmp_ge_i32_e32 vcc, s11, v6
	v_mov_b32_e32 v6, s69
	s_nop 0
	v_addc_co_u32_e32 v2, vcc, v2, v3, vcc
	v_cmp_ge_i32_e32 vcc, s11, v7
	s_nop 1
	v_cndmask_b32_e64 v3, 0, 1, vcc
	v_cmp_ge_i32_e32 vcc, s11, v8
	v_mov_b32_e32 v8, s70
	s_nop 0
	v_addc_co_u32_e32 v10, vcc, v2, v3, vcc
	v_mov_b32_e32 v2, s67
	ds_read2_b32 v[2:3], v2 offset1:1
	v_cmp_ge_i32_e32 vcc, s11, v9
	ds_read2_b32 v[4:5], v4 offset1:1
	ds_read2_b32 v[6:7], v6 offset1:1
	ds_read2_b32 v[8:9], v8 offset1:1
	v_cndmask_b32_e64 v11, 0, 1, vcc
	s_waitcnt lgkmcnt(0)
	v_cmp_ge_i32_e32 vcc, s11, v2
	s_nop 1
	v_addc_co_u32_e32 v2, vcc, v10, v11, vcc
	v_cmp_ge_i32_e32 vcc, s11, v3
	s_nop 1
	v_cndmask_b32_e64 v3, 0, 1, vcc
	v_cmp_ge_i32_e32 vcc, s11, v4
	v_mov_b32_e32 v4, s72
	s_nop 0
	v_addc_co_u32_e32 v2, vcc, v2, v3, vcc
	v_cmp_ge_i32_e32 vcc, s11, v5
	s_nop 1
	v_cndmask_b32_e64 v3, 0, 1, vcc
	v_cmp_ge_i32_e32 vcc, s11, v6
	v_mov_b32_e32 v6, s73
	s_nop 0
	v_addc_co_u32_e32 v2, vcc, v2, v3, vcc
	v_cmp_ge_i32_e32 vcc, s11, v7
	s_nop 1
	v_cndmask_b32_e64 v3, 0, 1, vcc
	v_cmp_ge_i32_e32 vcc, s11, v8
	v_mov_b32_e32 v8, s75
	s_nop 0
	v_addc_co_u32_e32 v10, vcc, v2, v3, vcc
	v_mov_b32_e32 v2, s71
	ds_read2_b32 v[2:3], v2 offset1:1
	v_cmp_ge_i32_e32 vcc, s11, v9
	ds_read2_b32 v[4:5], v4 offset1:1
	ds_read2_b32 v[6:7], v6 offset1:1
	ds_read2_b32 v[8:9], v8 offset1:1
	v_cndmask_b32_e64 v11, 0, 1, vcc
	s_waitcnt lgkmcnt(0)
	v_cmp_ge_i32_e32 vcc, s11, v2
	s_nop 1
	v_addc_co_u32_e32 v2, vcc, v10, v11, vcc
	v_cmp_ge_i32_e32 vcc, s11, v3
	v_mov_b32_e32 v10, s79
	s_nop 0
	v_cndmask_b32_e64 v3, 0, 1, vcc
	v_cmp_ge_i32_e32 vcc, s11, v4
	v_mov_b32_e32 v4, s77
	s_nop 0
	v_addc_co_u32_e32 v2, vcc, v2, v3, vcc
	v_cmp_ge_i32_e32 vcc, s11, v5
	s_nop 1
	v_cndmask_b32_e64 v3, 0, 1, vcc
	v_cmp_ge_i32_e32 vcc, s11, v6
	v_mov_b32_e32 v6, s78
	s_nop 0
	v_addc_co_u32_e32 v2, vcc, v2, v3, vcc
	v_cmp_ge_i32_e32 vcc, s11, v7
	s_nop 1
	v_cndmask_b32_e64 v3, 0, 1, vcc
	v_cmp_ge_i32_e32 vcc, s11, v8
	s_nop 1
	v_addc_co_u32_e32 v8, vcc, v2, v3, vcc
	v_mov_b32_e32 v2, s76
	ds_read2_b32 v[2:3], v2 offset1:1
	v_cmp_ge_i32_e32 vcc, s11, v9
	ds_read2_b32 v[4:5], v4 offset1:1
	ds_read2_b32 v[6:7], v6 offset1:1
	ds_read_b32 v10, v10
	v_cndmask_b32_e64 v9, 0, 1, vcc
	s_waitcnt lgkmcnt(0)
	v_cmp_ge_i32_e32 vcc, s11, v2
	s_nop 1
	v_addc_co_u32_e32 v2, vcc, v8, v9, vcc
	v_cmp_ge_i32_e32 vcc, s11, v3
	s_nop 1
	v_cndmask_b32_e64 v3, 0, 1, vcc
	v_cmp_ge_i32_e32 vcc, s11, v4
	s_nop 1
	v_addc_co_u32_e32 v2, vcc, v2, v3, vcc
	v_cmp_ge_i32_e32 vcc, s11, v5
	s_nop 1
	v_cndmask_b32_e64 v3, 0, 1, vcc
	v_cmp_ge_i32_e32 vcc, s11, v6
	s_nop 1
	v_addc_co_u32_e32 v2, vcc, v2, v3, vcc
	v_cmp_ge_i32_e32 vcc, s11, v7
	s_nop 1
	v_cndmask_b32_e64 v3, 0, 1, vcc
	v_cmp_ge_i32_e32 vcc, s11, v10
	s_nop 1
	v_addc_co_u32_e32 v2, vcc, v2, v3, vcc
	s_nop 0
	v_readfirstlane_b32 s34, v2
	s_mov_b64 s[38:39], -1
	s_and_b64 vcc, exec, s[8:9]
	s_cbranch_vccnz .LBB0_1447
